# P2: S^T and cross-term LDS fragment reads hoisted with register-ring renaming
# baseline (speedup 1.0000x reference)
.LBB0_259:
	ds_read_b128 v[62:65], v117
	ds_read_b128 v[66:69], v117 offset:8192
	ds_read_b128 v[174:177], v118
	ds_read_b128 v[178:181], v118 offset:8192
	ds_read_b128 v[182:185], v119
	ds_read_b128 v[186:189], v120
	s_nop 0
	v_mov_b32_e32 v4, v70
	v_mov_b32_e32 v5, v72
	s_waitcnt vmcnt(7)
	s_waitcnt lgkmcnt(5)
	v_mfma_f32_16x16x32_bf16 v[58:61], v[62:65], v[50:53], 0
	ds_read_b128 v[62:65], v119 offset:8192
	v_mov_b32_e32 v72, v71
	v_mov_b32_e32 v89, v88
	v_pk_mul_f32 v[20:21], v[88:89], v[20:21]
	s_nop 0
	s_waitcnt lgkmcnt(5)
	v_mfma_f32_16x16x32_bf16 v[50:53], v[66:69], v[50:53], 0
	ds_read_b128 v[66:69], v121
	v_pk_mul_f32 v[18:19], v[90:91], v[18:19]
	v_pk_mul_f32 v[16:17], v[88:89], v[16:17]
	s_waitcnt vmcnt(6)
	s_waitcnt lgkmcnt(5)
	v_mfma_f32_16x16x32_bf16 v[58:61], v[174:177], v[46:49], v[58:61]
	ds_read_b128 v[174:177], v120 offset:8192
	v_pk_mul_f32 v[14:15], v[90:91], v[14:15]
	v_lshl_add_u64 v[194:195], v[92:93], 0, s[20:21]
	s_nop 0
	s_waitcnt lgkmcnt(5)
	v_mfma_f32_16x16x32_bf16 v[46:49], v[178:181], v[46:49], v[50:53]
	ds_read_b128 v[178:181], v122
	s_nop 2
	v_pk_mul_f32 v[8:9], v[88:89], v[8:9]
	v_pk_mul_f32 v[6:7], v[90:91], v[6:7]
	s_waitcnt vmcnt(5)
	s_waitcnt lgkmcnt(5)
	v_mfma_f32_16x16x32_bf16 v[58:61], v[182:185], v[42:45], v[58:61]
	ds_read_b128 v[182:185], v121 offset:8192
	v_pk_mul_f32 v[12:13], v[88:89], v[12:13]
	v_pk_mul_f32 v[10:11], v[90:91], v[10:11]
	s_waitcnt vmcnt(4)
	s_waitcnt lgkmcnt(5)
	v_mfma_f32_16x16x32_bf16 v[50:53], v[186:189], v[38:41], v[58:61]
	ds_read_b128 v[186:189], v123
	s_nop 2
	s_add_i32 s22, s22, -1
	v_lshl_add_u64 v[92:93], v[92:93], 0, s[56:57]
	s_nop 0
	s_waitcnt lgkmcnt(5)
	v_mfma_f32_16x16x32_bf16 v[42:45], v[62:65], v[42:45], v[46:49]
	ds_read_b128 v[62:65], v122 offset:8192
	v_lshl_add_u64 v[94:95], v[94:95], 0, s[58:59]
	v_lshl_add_u64 v[96:97], v[96:97], 0, s[58:59]
	s_cmp_eq_u32 s22, 0
	s_waitcnt vmcnt(3)
	s_waitcnt lgkmcnt(5)
	v_mfma_f32_16x16x32_bf16 v[50:53], v[66:69], v[34:37], v[50:53]
	ds_read_b128 v[66:69], v124
	v_lshl_add_u64 v[98:99], v[98:99], 0, s[58:59]
	s_nop 0
	s_waitcnt lgkmcnt(5)
	v_mfma_f32_16x16x32_bf16 v[38:41], v[174:177], v[38:41], v[42:45]
	ds_read_b128 v[174:177], v123 offset:8192
	s_waitcnt vmcnt(2)
	s_waitcnt lgkmcnt(5)
	v_mfma_f32_16x16x32_bf16 v[50:53], v[178:181], v[30:33], v[50:53]
	ds_read_b128 v[190:193], v124 offset:8192
	s_nop 0
	s_waitcnt lgkmcnt(5)
	v_mfma_f32_16x16x32_bf16 v[34:37], v[182:185], v[34:37], v[38:41]
	s_waitcnt vmcnt(1)
	s_waitcnt lgkmcnt(4)
	v_mfma_f32_16x16x32_bf16 v[50:53], v[186:189], v[26:29], v[50:53]
	s_nop 0
	s_waitcnt lgkmcnt(3)
	v_mfma_f32_16x16x32_bf16 v[30:33], v[62:65], v[30:33], v[34:37]
	s_nop 3
	ds_read_b128 v[34:37], v125
	s_waitcnt vmcnt(0)
	s_waitcnt lgkmcnt(3)
	v_mfma_f32_16x16x32_bf16 v[50:53], v[66:69], v[22:25], v[50:53]
	s_nop 0
	s_waitcnt lgkmcnt(2)
	v_mfma_f32_16x16x32_bf16 v[26:29], v[174:177], v[26:29], v[30:33]
	s_nop 2
	ds_read_b128 v[30:33], v125 offset:4352
	ds_read_b64_tr_b16 v[38:39], v126
	ds_read_b64_tr_b16 v[40:41], v127 offset:1024
	v_mov_b32_e32 v66, v50
	v_mov_b32_e32 v67, v52
	v_mov_b32_e32 v52, v51
	v_pk_fma_f32 v[4:5], v[86:87], v[66:67], v[4:5]
	v_pk_fma_f32 v[50:51], v[86:87], v[52:53], v[72:73]
	v_and_b32_sdwa v46, v4, v159 dst_sel:DWORD dst_unused:UNUSED_PAD src0_sel:WORD_1 src1_sel:DWORD
	v_and_b32_sdwa v47, v51, v159 dst_sel:DWORD dst_unused:UNUSED_PAD src0_sel:WORD_1 src1_sel:DWORD
	v_and_b32_sdwa v48, v50, v159 dst_sel:DWORD dst_unused:UNUSED_PAD src0_sel:WORD_1 src1_sel:DWORD
	v_add3_u32 v62, v4, v46, s74
	v_add3_u32 v4, v51, v47, s74
	v_add3_u32 v63, v50, v48, s74
	s_waitcnt lgkmcnt(4)
	v_mfma_f32_16x16x32_bf16 v[22:25], v[190:193], v[22:25], v[26:29]
	s_nop 2
	ds_read_b128 v[26:29], v125 offset:64
	ds_read_b64_tr_b16 v[42:43], v127 offset:9216
	ds_read_b64_tr_b16 v[44:45], v127 offset:17408
	ds_read_b64_tr_b16 v[46:47], v128
	ds_read_b64_tr_b16 v[48:49], v129 offset:1024
	ds_read_b128 v[50:53], v125 offset:4416
	v_and_b32_sdwa v3, v5, v159 dst_sel:DWORD dst_unused:UNUSED_PAD src0_sel:WORD_1 src1_sel:DWORD
	s_waitcnt lgkmcnt(6)
	v_mfma_f32_16x16x32_bf16 v[18:21], v[34:37], v[38:41], v[18:21]
	v_add3_u32 v3, v5, v3, s74
	v_and_b32_e32 v64, 0xffff0000, v4
	v_mfma_f32_16x16x32_bf16 v[14:17], v[30:33], v[38:41], v[14:17]
	ds_read_b64_tr_b16 v[38:39], v129 offset:9216
	ds_read_b64_tr_b16 v[60:61], v127 offset:25600
	ds_read_b64_tr_b16 v[40:41], v130
	s_waitcnt lgkmcnt(4)
	v_mfma_f32_16x16x32_bf16 v[4:7], v[30:33], v[46:49], v[6:9]
	v_and_b32_e32 v32, 0xffff0000, v63
	v_or_b32_sdwa v33, v64, v3 dst_sel:DWORD dst_unused:UNUSED_PAD src0_sel:DWORD src1_sel:WORD_1
	v_or_b32_sdwa v32, v32, v62 dst_sel:DWORD dst_unused:UNUSED_PAD src0_sel:DWORD src1_sel:WORD_1
	s_waitcnt lgkmcnt(0)
	v_mfma_f32_16x16x32_bf16 v[18:21], v[26:29], v[40:43], v[18:21]
	v_mfma_f32_16x16x32_bf16 v[14:17], v[50:53], v[40:43], v[14:17]
	v_add_co_u32_e32 v40, vcc, s76, v194
	s_nop 1
	v_addc_co_u32_e32 v41, vcc, 0, v195, vcc
	v_mfma_f32_16x16x32_bf16 v[10:13], v[34:37], v[46:49], v[10:13]
	ds_read_b64_tr_b16 v[36:37], v131
	ds_read_b64_tr_b16 v[8:9], v129 offset:17408
	ds_read_b64_tr_b16 v[30:31], v129 offset:25600
	global_store_dwordx2 v[40:41], v[32:33], off
	ds_read_b128 v[32:35], v125 offset:128
	ds_read_b128 v[46:49], v125 offset:4480
	ds_read_b64_tr_b16 v[42:43], v132
	s_waitcnt lgkmcnt(5)
	v_mfma_f32_16x16x32_bf16 v[10:13], v[26:29], v[36:39], v[10:13]
	v_mov_b32_e32 v27, v24
	v_mov_b32_e32 v24, v23
	v_mov_b32_e32 v26, v22
	v_mfma_f32_16x16x32_bf16 v[36:39], v[50:53], v[36:39], v[4:7]
	ds_read_b128 v[50:53], v125 offset:192
	s_nop 1
	ds_read_b64_tr_b16 v[6:7], v133
	ds_read_b64_tr_b16 v[58:59], v134
	ds_read_b64_tr_b16 v[28:29], v135
	v_mov_b32_e32 v5, v56
	v_mov_b32_e32 v56, v55
	s_waitcnt lgkmcnt(4)
	v_mfma_f32_16x16x32_bf16 v[18:21], v[32:35], v[42:45], v[18:21]
	v_mov_b32_e32 v4, v54
	v_pk_fma_f32 v[22:23], v[86:87], v[24:25], v[56:57]
	v_pk_fma_f32 v[26:27], v[86:87], v[26:27], v[4:5]
	s_waitcnt lgkmcnt(1)
	v_mfma_f32_16x16x32_bf16 v[18:21], v[50:53], v[58:61], v[18:21]
	v_and_b32_sdwa v3, v27, v159 dst_sel:DWORD dst_unused:UNUSED_PAD src0_sel:WORD_1 src1_sel:DWORD
	v_and_b32_sdwa v24, v22, v159 dst_sel:DWORD dst_unused:UNUSED_PAD src0_sel:WORD_1 src1_sel:DWORD
	v_add3_u32 v3, v27, v3, s74
	v_mfma_f32_16x16x32_bf16 v[10:13], v[32:35], v[6:9], v[10:13]
	v_add3_u32 v22, v22, v24, s74
	v_and_b32_e32 v22, 0xffff0000, v22
	ds_read_b128 v[62:65], v125 offset:4544
	v_mfma_f32_16x16x32_bf16 v[4:7], v[46:49], v[6:9], v[36:39]
	v_and_b32_sdwa v9, v23, v159 dst_sel:DWORD dst_unused:UNUSED_PAD src0_sel:WORD_1 src1_sel:DWORD
	v_add3_u32 v9, v23, v9, s74
	v_and_b32_sdwa v8, v26, v159 dst_sel:DWORD dst_unused:UNUSED_PAD src0_sel:WORD_1 src1_sel:DWORD
	v_and_b32_e32 v9, 0xffff0000, v9
	v_add3_u32 v8, v26, v8, s74
	v_or_b32_sdwa v9, v9, v3 dst_sel:DWORD dst_unused:UNUSED_PAD src0_sel:DWORD src1_sel:WORD_1
	v_bfe_u32 v3, v18, 16, 1
	v_or_b32_sdwa v8, v22, v8 dst_sel:DWORD dst_unused:UNUSED_PAD src0_sel:DWORD src1_sel:WORD_1
	v_add3_u32 v3, v18, v3, s74
	global_store_dwordx2 v[40:41], v[8:9], off offset:32
	s_waitcnt lgkmcnt(0)
	s_barrier
	ds_write_b16_d16_hi v136, v3
	v_bfe_u32 v3, v19, 16, 1
	v_add3_u32 v3, v19, v3, s74
	v_mfma_f32_16x16x32_bf16 v[10:13], v[50:53], v[28:31], v[10:13]
	ds_write_b16_d16_hi v137, v3
	v_bfe_u32 v3, v20, 16, 1
	v_add3_u32 v3, v20, v3, s74
	ds_write_b16_d16_hi v138, v3
	v_bfe_u32 v3, v21, 16, 1
	v_add3_u32 v3, v21, v3, s74
	v_mfma_f32_16x16x32_bf16 v[14:17], v[46:49], v[42:45], v[14:17]
	ds_write_b16_d16_hi v139, v3
	v_bfe_u32 v3, v10, 16, 1
	v_add3_u32 v3, v10, v3, s74
	ds_write_b16_d16_hi v140, v3
	v_bfe_u32 v3, v11, 16, 1
	v_add3_u32 v3, v11, v3, s74
	v_mfma_f32_16x16x32_bf16 v[14:17], v[62:65], v[58:61], v[14:17]
	ds_write_b16_d16_hi v141, v3
	v_bfe_u32 v3, v12, 16, 1
	v_add3_u32 v3, v12, v3, s74
	ds_write_b16_d16_hi v142, v3
	v_bfe_u32 v3, v13, 16, 1
	v_add3_u32 v3, v13, v3, s74
	ds_write_b16_d16_hi v143, v3
	s_nop 0
	v_bfe_u32 v3, v14, 16, 1
	v_add3_u32 v3, v14, v3, s74
	ds_write_b16_d16_hi v136, v3 offset:8192
	v_bfe_u32 v3, v15, 16, 1
	v_add3_u32 v3, v15, v3, s74
	v_mfma_f32_16x16x32_bf16 v[6:9], v[62:65], v[28:31], v[4:7]
	ds_write_b16_d16_hi v144, v3 offset:8704
	v_bfe_u32 v3, v16, 16, 1
	v_add3_u32 v3, v16, v3, s74
	ds_write_b16_d16_hi v145, v3 offset:9216
	v_bfe_u32 v3, v17, 16, 1
	v_add3_u32 v3, v17, v3, s74
	ds_write_b16_d16_hi v146, v3 offset:9728
	s_nop 0
	v_bfe_u32 v3, v6, 16, 1
	v_add3_u32 v3, v6, v3, s74
	ds_write_b16_d16_hi v140, v3 offset:8192
	v_bfe_u32 v3, v7, 16, 1
	v_add3_u32 v3, v7, v3, s74
	ds_write_b16_d16_hi v147, v3 offset:8704
	v_bfe_u32 v3, v8, 16, 1
	v_add3_u32 v3, v8, v3, s74
	ds_write_b16_d16_hi v148, v3 offset:9216
	v_bfe_u32 v3, v9, 16, 1
	v_add3_u32 v3, v9, v3, s74
	ds_write_b16_d16_hi v149, v3 offset:9728
	s_cbranch_scc1 .LBB0_251
